# B4 (layer 0): compute workgroups capped at 192 so 64 workgroups serve the weight-conversion queue while the expert GEMM runs
# speedup vs baseline: 1.0060x; 1.0060x over previous
.LBB0_1419:
	v_writelane_b32 v253, s62, 40
	s_nop 1
	v_writelane_b32 v253, s63, 41
	v_writelane_b32 v253, s61, 62
	s_or_b64 exec, exec, s[0:1]
	v_readlane_b32 s8, v253, 31
	v_readlane_b32 s9, v253, 32
	s_waitcnt lgkmcnt(0)
	s_barrier
	v_readlane_b32 s10, v253, 12
	v_readlane_b32 s11, v253, 13
	s_nop 0
	global_load_dword v0, v173, s[8:9] sc1
	global_load_dword v1, v173, s[8:9] offset:256 sc1
	global_load_dword v2, v173, s[8:9] offset:512 sc1
	global_load_dword v3, v173, s[8:9] offset:768 sc1
	global_load_dword v4, v173, s[8:9] offset:1024 sc1
	global_load_dword v5, v173, s[8:9] offset:1280 sc1
	global_load_dword v6, v173, s[8:9] offset:1536 sc1
	global_load_dword v7, v173, s[8:9] offset:1792 sc1
	v_readlane_b32 s30, v253, 9
	s_waitcnt vmcnt(0)
	v_readfirstlane_b32 s0, v0
	s_nop 0
	s_min_i32 s0, s0, 0x2000
	s_addk_i32 s0, 0xff
	s_ashr_i32 s2, s0, 8
	s_nop 0
	v_readfirstlane_b32 s0, v1
	s_nop 0
	s_min_i32 s0, s0, 0x2000
	s_addk_i32 s0, 0xff
	s_ashr_i32 s3, s0, 8
	s_add_i32 s7, s3, s2
	s_nop 0
	v_readfirstlane_b32 s0, v2
	s_nop 0
	s_min_i32 s0, s0, 0x2000
	s_addk_i32 s0, 0xff
	s_ashr_i32 s73, s0, 8
	s_add_i32 s61, s73, s7
	s_nop 0
	v_readfirstlane_b32 s0, v3
	s_nop 0
	s_min_i32 s0, s0, 0x2000
	s_addk_i32 s0, 0xff
	s_ashr_i32 s74, s0, 8
	s_add_i32 s62, s74, s61
	s_nop 0
	v_readfirstlane_b32 s0, v4
	s_nop 0
	s_min_i32 s0, s0, 0x2000
	s_addk_i32 s0, 0xff
	s_ashr_i32 s75, s0, 8
	s_add_i32 s63, s75, s62
	s_nop 0
	v_readfirstlane_b32 s0, v5
	s_nop 0
	s_min_i32 s0, s0, 0x2000
	s_addk_i32 s0, 0xff
	s_ashr_i32 s84, s0, 8
	s_add_i32 s64, s84, s63
	s_nop 0
	v_readfirstlane_b32 s0, v6
	s_nop 0
	s_min_i32 s0, s0, 0x2000
	s_addk_i32 s0, 0xff
	s_ashr_i32 s65, s0, 8
	s_add_i32 s43, s65, s64
	s_nop 0
	v_readfirstlane_b32 s0, v7
	s_min_i32 s0, s0, 0x2000
	s_addk_i32 s0, 0xff
	s_ashr_i32 s66, s0, 8
	s_add_i32 s0, s66, s43
	s_cmp_lt_i32 s0, 1
	s_mul_i32 s8, s0, 11
	s_cselect_b64 s[0:1], -1, 0
	s_or_b64 s[0:1], s[10:11], s[0:1]
	s_and_b64 vcc, exec, s[0:1]
	s_cbranch_vccnz .LBB0_1421
	s_add_i32 s0, s8, -1
	v_readlane_b32 s13, v253, 9
	s_add_i32 s1, s0, s13
	s_ashr_i32 s9, s1, 31
	v_readlane_b32 s10, v253, 29
	s_xor_b32 s9, s9, s10
	s_abs_i32 s1, s1
	v_readlane_b32 s10, v253, 49
	s_mul_hi_u32 s10, s1, s10
	v_readlane_b32 s14, v253, 50
	s_mul_i32 s11, s10, s14
	s_sub_i32 s1, s1, s11
	s_add_i32 s11, s10, 1
	s_sub_i32 s12, s1, s14
	s_cmp_ge_u32 s1, s14
	s_cselect_b32 s10, s11, s10
	s_cselect_b32 s1, s12, s1
	s_add_i32 s11, s10, 1
	s_cmp_ge_u32 s1, s14
	s_cselect_b32 s1, s11, s10
	s_xor_b32 s1, s1, s9
	s_sub_i32 s1, s1, s9
	s_abs_i32 s9, s1
	v_cvt_f32_u32_e32 v0, s9
	s_sub_i32 s10, 0, s9
	s_add_i32 s0, s1, s0
	s_xor_b32 s1, s0, s1
	v_rcp_iflag_f32_e32 v0, v0
	s_abs_i32 s0, s0
	s_ashr_i32 s1, s1, 31
	v_mul_f32_e32 v0, 0x4f7ffffe, v0
	v_cvt_u32_f32_e32 v0, v0
	s_nop 0
	v_readfirstlane_b32 s11, v0
	s_mul_i32 s10, s10, s11
	s_mul_hi_u32 s10, s11, s10
	s_add_i32 s11, s11, s10
	s_mul_hi_u32 s10, s0, s11
	s_mul_i32 s11, s10, s9
	s_sub_i32 s0, s0, s11
	s_add_i32 s11, s10, 1
	s_sub_i32 s12, s0, s9
	s_cmp_ge_u32 s0, s9
	s_cselect_b32 s10, s11, s10
	s_cselect_b32 s0, s12, s0
	s_add_i32 s11, s10, 1
	s_cmp_ge_u32 s0, s9
	s_cselect_b32 s0, s11, s10
	s_xor_b32 s0, s0, s1
	s_sub_i32 s0, s0, s1
	s_add_i32 s0, s0, 7
	s_and_b32 s0, s0, -8
	s_min_i32 s30, s0, s13
	s_min_i32 s30, s30, 0xc0
